# prologue de-serialisation: int8 w_in transpose items issue the 8 weight-row loads before waiting on the 4 column-max loads (one round trip per item instead of two)
# baseline (speedup 1.0000x reference)
; #define LAS __attribute__((address_space(3)))
; #define LDS_WAIT() asm volatile("s_waitcnt lgkmcnt(0)" ::: "memory")
; __device__ __forceinline__ void transpose_item_i8(const float* W, int ldw, int K, unsigned char* WT8, LAS float* scr, int kb, int nb, int lane, const unsigned* CM, float* SW) {
;     const int k0 = 64 * kb, n0 = 32 * nb;
;     const int n4 = (lane & 7) * 4, kr = lane >> 3;
;     f32x4 inv;
; #pragma unroll
;     for (int e = 0; e < 4; ++e) { const float cm = __uint_as_float(__hip_atomic_load((unsigned*)CM + n0 + n4 + e, __ATOMIC_RELAXED, __HIP_MEMORY_SCOPE_AGENT)); inv[e] = (cm > 0.f) ? 127.0f / cm : 0.f; if (kb == 0 && kr == 0) SW[n0 + n4 + e] = cm * (1.0f / 127.0f); }
; #pragma unroll
;     for (int i = 0; i < 8; ++i) { const int kk = 8 * i + kr; const f32x4 v = __builtin_nontemporal_load((const f32x4*)(W + (size_t)(k0 + kk) * ldw + n0 + n4)) * inv;
;         scr[kk * 33 + n4] = v[0]; scr[kk * 33 + n4 + 1] = v[1]; scr[kk * 33 + n4 + 2] = v[2]; scr[kk * 33 + n4 + 3] = v[3]; }
;     LDS_WAIT();
.LBB0_155:
	s_or_b64 exec, exec, s[26:27]
	s_lshl_b32 s24, s41, 6
	v_lshl_add_u64 v[20:21], s[22:23], 2, v[10:11]
	v_or_b32_e32 v44, s24, v34
	v_mad_i64_i32 v[44:45], s[26:27], v44, s35, v[20:21]
	v_or_b32_e32 v48, s24, v35
	global_load_dwordx4 v[44:47], v[44:45], off nt
	v_mad_i64_i32 v[48:49], s[26:27], v48, s35, v[20:21]
	v_or_b32_e32 v58, s24, v52
	global_load_dwordx4 v[48:51], v[48:49], off nt
	v_mad_i64_i32 v[58:59], s[26:27], v58, s35, v[20:21]
	v_or_b32_e32 v62, s24, v53
	global_load_dwordx4 v[58:61], v[58:59], off nt
	v_mad_i64_i32 v[62:63], s[26:27], v62, s35, v[20:21]
	v_or_b32_e32 v66, s24, v54
	global_load_dwordx4 v[62:65], v[62:63], off nt
	v_mad_i64_i32 v[66:67], s[26:27], v66, s35, v[20:21]
	v_or_b32_e32 v70, s24, v55
	global_load_dwordx4 v[66:69], v[66:67], off nt
	v_mad_i64_i32 v[70:71], s[26:27], v70, s35, v[20:21]
	v_or_b32_e32 v74, s24, v56
	v_or_b32_e32 v78, s24, v57
	global_load_dwordx4 v[70:73], v[70:71], off nt
	v_mad_i64_i32 v[74:75], s[26:27], v74, s35, v[20:21]
	v_mad_i64_i32 v[20:21], s[26:27], v78, s35, v[20:21]
	global_load_dwordx4 v[74:77], v[74:75], off nt
	global_load_dwordx4 v[78:81], v[20:21], off nt
	s_ashr_i32 s25, s24, 31
	s_add_i32 s40, s40, s14
	s_add_i32 s6, s6, s49
	s_cmpk_gt_i32 s40, 0x17ff
	s_waitcnt vmcnt(8)
	v_div_scale_f32 v15, s[26:27], v41, v41, s34
	v_rcp_f32_e32 v82, v15
	v_div_scale_f32 v83, vcc, s34, v41, s34
	v_fma_f32 v130, -v15, v82, 1.0
	v_fmac_f32_e32 v82, v130, v82
	v_mul_f32_e32 v130, v83, v82
	v_fma_f32 v131, -v15, v130, v83
	v_fmac_f32_e32 v130, v131, v82
	v_fma_f32 v15, -v15, v130, v83
	v_div_fmas_f32 v15, v15, v82, v130
	v_div_fixup_f32 v15, v15, v41, s34
	v_cmp_lt_f32_e32 vcc, 0, v41
	v_cndmask_b32_e32 v20, 0, v15, vcc
	v_div_scale_f32 v15, s[26:27], v42, v42, s34
	v_rcp_f32_e32 v82, v15
	v_div_scale_f32 v83, vcc, s34, v42, s34
	v_fma_f32 v130, -v15, v82, 1.0
	v_fmac_f32_e32 v82, v130, v82
	v_mul_f32_e32 v130, v83, v82
	v_fma_f32 v131, -v15, v130, v83
	v_fmac_f32_e32 v130, v131, v82
	v_fma_f32 v15, -v15, v130, v83
	v_div_fmas_f32 v15, v15, v82, v130
	v_div_fixup_f32 v15, v15, v42, s34
	v_cmp_lt_f32_e32 vcc, 0, v42
	v_cndmask_b32_e32 v21, 0, v15, vcc
	v_div_scale_f32 v15, s[26:27], v43, v43, s34
	v_rcp_f32_e32 v82, v15
	v_div_scale_f32 v83, vcc, s34, v43, s34
	v_fma_f32 v130, -v15, v82, 1.0
	v_fmac_f32_e32 v82, v130, v82
	v_mul_f32_e32 v130, v83, v82
	v_fma_f32 v131, -v15, v130, v83
	v_fmac_f32_e32 v130, v131, v82
	v_fma_f32 v15, -v15, v130, v83
	v_div_fmas_f32 v15, v15, v82, v130
	v_div_fixup_f32 v15, v15, v43, s34
	v_cmp_lt_f32_e32 vcc, 0, v43
	v_cndmask_b32_e32 v42, 0, v15, vcc
	v_div_scale_f32 v15, s[26:27], v14, v14, s34
	v_rcp_f32_e32 v82, v15
	v_div_scale_f32 v83, vcc, s34, v14, s34
	v_fma_f32 v130, -v15, v82, 1.0
	v_fmac_f32_e32 v82, v130, v82
	v_mul_f32_e32 v130, v83, v82
	v_fma_f32 v131, -v15, v130, v83
	v_fmac_f32_e32 v130, v131, v82
	v_fma_f32 v15, -v15, v130, v83
	v_div_fmas_f32 v15, v15, v82, v130
	v_div_fixup_f32 v15, v15, v14, s34
	v_cmp_lt_f32_e32 vcc, 0, v14
	v_cndmask_b32_e32 v43, 0, v15, vcc
	v_add_u32_e32 v82, s22, v18
	v_ashrrev_i32_e32 v83, 31, v82
	s_waitcnt vmcnt(7)
	v_pk_mul_f32 v[44:45], v[20:21], v[44:45]
	v_pk_mul_f32 v[14:15], v[42:43], v[46:47]
	ds_write2_b32 v1, v44, v45 offset1:1
	ds_write2_b32 v1, v14, v15 offset0:2 offset1:3
	s_waitcnt vmcnt(6)
	v_pk_mul_f32 v[14:15], v[42:43], v[50:51]
	v_pk_mul_f32 v[44:45], v[20:21], v[48:49]
	ds_write2_b32 v23, v44, v45 offset1:1
	ds_write2_b32 v24, v14, v15 offset1:1
	s_waitcnt vmcnt(5)
	v_pk_mul_f32 v[14:15], v[42:43], v[60:61]
	v_pk_mul_f32 v[44:45], v[20:21], v[58:59]
	ds_write2_b32 v25, v44, v45 offset1:1
	ds_write2_b32 v26, v14, v15 offset1:1
	s_waitcnt vmcnt(4)
	v_pk_mul_f32 v[14:15], v[42:43], v[64:65]
	v_pk_mul_f32 v[44:45], v[20:21], v[62:63]
	ds_write2_b32 v27, v44, v45 offset1:1
	ds_write2_b32 v28, v14, v15 offset1:1
	s_waitcnt vmcnt(3)
	v_pk_mul_f32 v[14:15], v[42:43], v[68:69]
	v_pk_mul_f32 v[44:45], v[20:21], v[66:67]
	ds_write2_b32 v29, v44, v45 offset1:1
	ds_write2_b32 v30, v14, v15 offset1:1
	s_waitcnt vmcnt(2)
	v_pk_mul_f32 v[14:15], v[42:43], v[72:73]
	v_pk_mul_f32 v[44:45], v[20:21], v[70:71]
	ds_write2_b32 v31, v44, v45 offset1:1
	ds_write2_b32 v32, v14, v15 offset1:1
	s_waitcnt vmcnt(1)
	v_pk_mul_f32 v[14:15], v[42:43], v[76:77]
	v_pk_mul_f32 v[44:45], v[20:21], v[74:75]
	s_waitcnt vmcnt(0)
	v_pk_mul_f32 v[20:21], v[20:21], v[78:79]
	ds_write2_b32 v33, v44, v45 offset1:1
	ds_write2_b32 v37, v14, v15 offset1:1
	v_pk_mul_f32 v[14:15], v[42:43], v[80:81]
	ds_write2_b32 v38, v20, v21 offset1:1
	ds_write2_b32 v39, v14, v15 offset1:1
	s_waitcnt lgkmcnt(0)
	ds_read2_b32 v[14:15], v22 offset1:16
	ds_read2_b32 v[46:47], v22 offset0:33 offset1:49
	ds_read2_b32 v[48:49], v22 offset0:66 offset1:82
	ds_read2_b32 v[50:51], v22 offset0:99 offset1:115
	ds_read2_b32 v[58:59], v22 offset0:132 offset1:148
	ds_read2_b32 v[60:61], v22 offset0:165 offset1:181
	ds_read2_b32 v[62:63], v22 offset0:198 offset1:214
	ds_read2_b32 v[64:65], v22 offset0:231 offset1:247
	s_waitcnt lgkmcnt(6)
; #define LAS __attribute__((address_space(3)))
; #define LDS_WAIT() asm volatile("s_waitcnt lgkmcnt(0)" ::: "memory")
; __device__ __forceinline__ void transpose_item_i8(const float* W, int ldw, int K, unsigned char* WT8, LAS float* scr, int kb, int nb, int lane, const unsigned* CM, float* SW) {
;     ...
;     const int c = lane & 3;
; #pragma unroll
;     for (int j = 0; j < 2; ++j) { const int n = (lane >> 2) + 16 * j; const LAS float* sp = scr + (16 * c) * 33 + n;
;         v4u o; o.x = pk4_i8(sp[0 * 33], sp[1 * 33], sp[2 * 33], sp[3 * 33]); o.y = pk4_i8(sp[4 * 33], sp[5 * 33], sp[6 * 33], sp[7 * 33]);
;         o.z = pk4_i8(sp[8 * 33], sp[9 * 33], sp[10 * 33], sp[11 * 33]); o.w = pk4_i8(sp[12 * 33], sp[13 * 33], sp[14 * 33], sp[15 * 33]);
;         *(v4u*)(WT8 + (size_t)(n0 + n) * K + k0 + 16 * c) = o; }
;     LDS_WAIT();
	v_rndne_f32_e32 v41, v46
	v_rndne_f32_e32 v14, v14
	v_cvt_i32_f32_e32 v41, v41
	s_waitcnt lgkmcnt(5)
	v_rndne_f32_e32 v42, v48
	v_cvt_i32_f32_e32 v14, v14
	v_cvt_i32_f32_sdwa v42, v42 dst_sel:WORD_1 dst_unused:UNUSED_PAD src0_sel:DWORD
	s_waitcnt lgkmcnt(4)
	v_rndne_f32_e32 v43, v50
	v_cvt_i32_f32_sdwa v43, v43 dst_sel:BYTE_3 dst_unused:UNUSED_PAD src0_sel:DWORD
	v_lshlrev_b32_e32 v41, 8, v41
	v_perm_b32 v14, v41, v14, s36
	v_and_b32_e32 v41, 0xff0000, v42
	v_or3_b32 v42, v14, v41, v43
	s_waitcnt lgkmcnt(2)
	v_rndne_f32_e32 v41, v60
	v_rndne_f32_e32 v14, v58
	v_cvt_i32_f32_e32 v41, v41
	s_waitcnt lgkmcnt(1)
	v_rndne_f32_e32 v43, v62
	v_cvt_i32_f32_e32 v14, v14
	v_cvt_i32_f32_sdwa v43, v43 dst_sel:WORD_1 dst_unused:UNUSED_PAD src0_sel:DWORD
	s_waitcnt lgkmcnt(0)
	v_rndne_f32_e32 v44, v64
	v_cvt_i32_f32_sdwa v44, v44 dst_sel:BYTE_3 dst_unused:UNUSED_PAD src0_sel:DWORD
	ds_read2_b32 v[66:67], v40 offset0:8 offset1:24
	ds_read2_b32 v[68:69], v40 offset0:41 offset1:57
	ds_read2_b32 v[70:71], v40 offset0:74 offset1:90
	ds_read2_b32 v[72:73], v40 offset0:107 offset1:123
	v_lshlrev_b32_e32 v41, 8, v41
	v_perm_b32 v14, v41, v14, s36
	v_and_b32_e32 v41, 0xff0000, v43
	v_or3_b32 v43, v14, v41, v44
	s_waitcnt lgkmcnt(2)
	v_rndne_f32_e32 v41, v68
	v_rndne_f32_e32 v14, v66
	v_cvt_i32_f32_e32 v41, v41
	s_waitcnt lgkmcnt(1)
	v_rndne_f32_e32 v44, v70
	v_cvt_i32_f32_e32 v14, v14
	v_cvt_i32_f32_sdwa v44, v44 dst_sel:WORD_1 dst_unused:UNUSED_PAD src0_sel:DWORD
	s_waitcnt lgkmcnt(0)
	v_rndne_f32_e32 v45, v72
	v_cvt_i32_f32_sdwa v45, v45 dst_sel:BYTE_3 dst_unused:UNUSED_PAD src0_sel:DWORD
	ds_read2_b32 v[74:75], v40 offset0:140 offset1:156
	ds_read2_b32 v[76:77], v40 offset0:173 offset1:189
	ds_read2_b32 v[78:79], v40 offset0:206 offset1:222
	ds_read2_b32 v[80:81], v40 offset0:239 offset1:255
	v_lshlrev_b32_e32 v41, 8, v41
	v_perm_b32 v14, v41, v14, s36
	v_and_b32_e32 v41, 0xff0000, v44
	v_or3_b32 v44, v14, v41, v45
	s_waitcnt lgkmcnt(2)
	v_rndne_f32_e32 v41, v76
	v_rndne_f32_e32 v14, v74
	v_cvt_i32_f32_e32 v41, v41
	s_waitcnt lgkmcnt(1)
	v_rndne_f32_e32 v45, v78
	v_cvt_i32_f32_e32 v14, v14
	v_cvt_i32_f32_sdwa v45, v45 dst_sel:WORD_1 dst_unused:UNUSED_PAD src0_sel:DWORD
	s_waitcnt lgkmcnt(0)
	v_rndne_f32_e32 v46, v80
	v_cvt_i32_f32_sdwa v46, v46 dst_sel:BYTE_3 dst_unused:UNUSED_PAD src0_sel:DWORD
	v_lshlrev_b32_e32 v41, 8, v41
	v_perm_b32 v14, v41, v14, s36
	v_and_b32_e32 v41, 0xff0000, v45
	v_lshl_add_u64 v[20:21], v[12:13], 0, s[24:25]
	v_or3_b32 v45, v14, v41, v46
	v_lshlrev_b64 v[84:85], 11, v[82:83]
	v_rndne_f32_e32 v14, v15
	v_rndne_f32_e32 v15, v47
	v_lshl_add_u64 v[84:85], v[20:21], 0, v[84:85]
	v_cvt_i32_f32_e32 v15, v15
	v_rndne_f32_e32 v41, v49
	global_store_dwordx4 v[84:85], v[42:45], off
	v_cvt_i32_f32_e32 v14, v14
	v_cvt_i32_f32_sdwa v41, v41 dst_sel:WORD_1 dst_unused:UNUSED_PAD src0_sel:DWORD
	v_rndne_f32_e32 v42, v51
	v_cvt_i32_f32_sdwa v42, v42 dst_sel:BYTE_3 dst_unused:UNUSED_PAD src0_sel:DWORD
	v_lshlrev_b32_e32 v15, 8, v15
	v_perm_b32 v14, v15, v14, s36
	v_and_b32_e32 v15, 0xff0000, v41
	v_or3_b32 v42, v14, v15, v42
	v_rndne_f32_e32 v15, v61
	v_rndne_f32_e32 v14, v59
	v_cvt_i32_f32_e32 v15, v15
	v_rndne_f32_e32 v41, v63
	v_cvt_i32_f32_e32 v14, v14
	v_cvt_i32_f32_sdwa v41, v41 dst_sel:WORD_1 dst_unused:UNUSED_PAD src0_sel:DWORD
	v_rndne_f32_e32 v43, v65
	v_cvt_i32_f32_sdwa v43, v43 dst_sel:BYTE_3 dst_unused:UNUSED_PAD src0_sel:DWORD
	v_lshlrev_b32_e32 v15, 8, v15
	v_perm_b32 v14, v15, v14, s36
	v_and_b32_e32 v15, 0xff0000, v41
	v_or3_b32 v43, v14, v15, v43
	v_rndne_f32_e32 v15, v69
	v_rndne_f32_e32 v14, v67
	v_cvt_i32_f32_e32 v15, v15
	v_rndne_f32_e32 v41, v71
	v_cvt_i32_f32_e32 v14, v14
	v_cvt_i32_f32_sdwa v41, v41 dst_sel:WORD_1 dst_unused:UNUSED_PAD src0_sel:DWORD
	v_rndne_f32_e32 v44, v73
	v_cvt_i32_f32_sdwa v44, v44 dst_sel:BYTE_3 dst_unused:UNUSED_PAD src0_sel:DWORD
	v_lshlrev_b32_e32 v15, 8, v15
	v_perm_b32 v14, v15, v14, s36
	v_and_b32_e32 v15, 0xff0000, v41
	v_or3_b32 v44, v14, v15, v44
	v_rndne_f32_e32 v15, v77
	v_rndne_f32_e32 v14, v75
	v_cvt_i32_f32_e32 v15, v15
	v_rndne_f32_e32 v41, v79
	v_cvt_i32_f32_e32 v14, v14
	v_cvt_i32_f32_sdwa v41, v41 dst_sel:WORD_1 dst_unused:UNUSED_PAD src0_sel:DWORD
	v_rndne_f32_e32 v45, v81
	v_cvt_i32_f32_sdwa v45, v45 dst_sel:BYTE_3 dst_unused:UNUSED_PAD src0_sel:DWORD
	v_lshlrev_b32_e32 v15, 8, v15
	v_perm_b32 v14, v15, v14, s36
	v_and_b32_e32 v15, 0xff0000, v41
	v_or3_b32 v45, v14, v15, v45
	v_add_u32_e32 v14, 16, v82
	v_ashrrev_i32_e32 v15, 31, v14
	v_lshlrev_b64 v[14:15], 11, v[14:15]
	v_lshl_add_u64 v[14:15], v[20:21], 0, v[14:15]
	global_store_dwordx4 v[14:15], v[42:45], off
	s_waitcnt lgkmcnt(0)
	s_cbranch_scc1 .LBB0_164

; #define LAS __attribute__((address_space(3)))
; #define LDS_WAIT() asm volatile("s_waitcnt lgkmcnt(0)" ::: "memory")
; __device__ __forceinline__ void transpose_item_i8(const float* W, int ldw, int K, unsigned char* WT8, LAS float* scr, int kb, int nb, int lane, const unsigned* CM, float* SW) {
;     const int k0 = 64 * kb, n0 = 32 * nb;
;     const int n4 = (lane & 7) * 4, kr = lane >> 3;
;     f32x4 inv;
; #pragma unroll
;     for (int e = 0; e < 4; ++e) { const float cm = __uint_as_float(__hip_atomic_load((unsigned*)CM + n0 + n4 + e, __ATOMIC_RELAXED, __HIP_MEMORY_SCOPE_AGENT)); inv[e] = (cm > 0.f) ? 127.0f / cm : 0.f; if (kb == 0 && kr == 0) SW[n0 + n4 + e] = cm * (1.0f / 127.0f); }
; #pragma unroll
;     for (int i = 0; i < 8; ++i) { const int kk = 8 * i + kr; const f32x4 v = __builtin_nontemporal_load((const f32x4*)(W + (size_t)(k0 + kk) * ldw + n0 + n4)) * inv;
;         scr[kk * 33 + n4] = v[0]; scr[kk * 33 + n4 + 1] = v[1]; scr[kk * 33 + n4 + 2] = v[2]; scr[kk * 33 + n4 + 3] = v[3]; }
;     LDS_WAIT();
.LBB0_168:
	s_or_b64 exec, exec, s[22:23]
	s_lshl_b32 s20, s25, 6
	v_lshl_add_u64 v[20:21], s[18:19], 2, v[10:11]
	v_or_b32_e32 v44, s20, v34
	v_mad_i64_i32 v[44:45], s[22:23], v44, s37, v[20:21]
	v_or_b32_e32 v48, s20, v35
	global_load_dwordx4 v[44:47], v[44:45], off nt
	v_mad_i64_i32 v[48:49], s[22:23], v48, s37, v[20:21]
	v_or_b32_e32 v58, s20, v52
	global_load_dwordx4 v[48:51], v[48:49], off nt
	v_mad_i64_i32 v[58:59], s[22:23], v58, s37, v[20:21]
	v_or_b32_e32 v62, s20, v53
	global_load_dwordx4 v[58:61], v[58:59], off nt
	v_mad_i64_i32 v[62:63], s[22:23], v62, s37, v[20:21]
	v_or_b32_e32 v66, s20, v54
	global_load_dwordx4 v[62:65], v[62:63], off nt
	v_mad_i64_i32 v[66:67], s[22:23], v66, s37, v[20:21]
	v_or_b32_e32 v70, s20, v55
	global_load_dwordx4 v[66:69], v[66:67], off nt
	v_mad_i64_i32 v[70:71], s[22:23], v70, s37, v[20:21]
	v_or_b32_e32 v74, s20, v56
	v_or_b32_e32 v78, s20, v57
	global_load_dwordx4 v[70:73], v[70:71], off nt
	v_mad_i64_i32 v[74:75], s[22:23], v74, s37, v[20:21]
	v_mad_i64_i32 v[20:21], s[22:23], v78, s37, v[20:21]
	global_load_dwordx4 v[74:77], v[74:75], off nt
	global_load_dwordx4 v[78:81], v[20:21], off nt
	s_ashr_i32 s21, s20, 31
	s_add_i32 s24, s24, s14
	s_add_i32 s6, s6, s49
	s_cmpk_gt_i32 s24, 0x17ff
	s_waitcnt vmcnt(8)
	v_div_scale_f32 v15, s[22:23], v41, v41, s34
	v_rcp_f32_e32 v82, v15
	v_div_scale_f32 v83, vcc, s34, v41, s34
	v_fma_f32 v130, -v15, v82, 1.0
	v_fmac_f32_e32 v82, v130, v82
	v_mul_f32_e32 v130, v83, v82
	v_fma_f32 v131, -v15, v130, v83
	v_fmac_f32_e32 v130, v131, v82
	v_fma_f32 v15, -v15, v130, v83
	v_div_fmas_f32 v15, v15, v82, v130
	v_div_fixup_f32 v15, v15, v41, s34
	v_cmp_lt_f32_e32 vcc, 0, v41
	v_cndmask_b32_e32 v20, 0, v15, vcc
	v_div_scale_f32 v15, s[22:23], v42, v42, s34
	v_rcp_f32_e32 v82, v15
	v_div_scale_f32 v83, vcc, s34, v42, s34
	v_fma_f32 v130, -v15, v82, 1.0
	v_fmac_f32_e32 v82, v130, v82
	v_mul_f32_e32 v130, v83, v82
	v_fma_f32 v131, -v15, v130, v83
	v_fmac_f32_e32 v130, v131, v82
	v_fma_f32 v15, -v15, v130, v83
	v_div_fmas_f32 v15, v15, v82, v130
	v_div_fixup_f32 v15, v15, v42, s34
	v_cmp_lt_f32_e32 vcc, 0, v42
	v_cndmask_b32_e32 v21, 0, v15, vcc
	v_div_scale_f32 v15, s[22:23], v43, v43, s34
	v_rcp_f32_e32 v82, v15
	v_div_scale_f32 v83, vcc, s34, v43, s34
	v_fma_f32 v130, -v15, v82, 1.0
	v_fmac_f32_e32 v82, v130, v82
	v_mul_f32_e32 v130, v83, v82
	v_fma_f32 v131, -v15, v130, v83
	v_fmac_f32_e32 v130, v131, v82
	v_fma_f32 v15, -v15, v130, v83
	v_div_fmas_f32 v15, v15, v82, v130
	v_div_fixup_f32 v15, v15, v43, s34
	v_cmp_lt_f32_e32 vcc, 0, v43
	v_cndmask_b32_e32 v42, 0, v15, vcc
	v_div_scale_f32 v15, s[22:23], v14, v14, s34
	v_rcp_f32_e32 v82, v15
	v_div_scale_f32 v83, vcc, s34, v14, s34
	v_fma_f32 v130, -v15, v82, 1.0
	v_fmac_f32_e32 v82, v130, v82
	v_mul_f32_e32 v130, v83, v82
	v_fma_f32 v131, -v15, v130, v83
	v_fmac_f32_e32 v130, v131, v82
	v_fma_f32 v15, -v15, v130, v83
	v_div_fmas_f32 v15, v15, v82, v130
	v_div_fixup_f32 v15, v15, v14, s34
	v_cmp_lt_f32_e32 vcc, 0, v14
	v_cndmask_b32_e32 v43, 0, v15, vcc
	v_add_u32_e32 v82, s18, v18
	v_ashrrev_i32_e32 v83, 31, v82
	s_waitcnt vmcnt(7)
	v_pk_mul_f32 v[44:45], v[20:21], v[44:45]
	v_pk_mul_f32 v[14:15], v[42:43], v[46:47]
	ds_write2_b32 v1, v44, v45 offset1:1
	ds_write2_b32 v1, v14, v15 offset0:2 offset1:3
	s_waitcnt vmcnt(6)
	v_pk_mul_f32 v[14:15], v[42:43], v[50:51]
	v_pk_mul_f32 v[44:45], v[20:21], v[48:49]
	ds_write2_b32 v23, v44, v45 offset1:1
	ds_write2_b32 v24, v14, v15 offset1:1
	s_waitcnt vmcnt(5)
	v_pk_mul_f32 v[14:15], v[42:43], v[60:61]
	v_pk_mul_f32 v[44:45], v[20:21], v[58:59]
	ds_write2_b32 v25, v44, v45 offset1:1
	ds_write2_b32 v26, v14, v15 offset1:1
	s_waitcnt vmcnt(4)
	v_pk_mul_f32 v[14:15], v[42:43], v[64:65]
	v_pk_mul_f32 v[44:45], v[20:21], v[62:63]
	ds_write2_b32 v27, v44, v45 offset1:1
	ds_write2_b32 v28, v14, v15 offset1:1
	s_waitcnt vmcnt(3)
	v_pk_mul_f32 v[14:15], v[42:43], v[68:69]
	v_pk_mul_f32 v[44:45], v[20:21], v[66:67]
	ds_write2_b32 v29, v44, v45 offset1:1
	ds_write2_b32 v30, v14, v15 offset1:1
	s_waitcnt vmcnt(2)
	v_pk_mul_f32 v[14:15], v[42:43], v[72:73]
	v_pk_mul_f32 v[44:45], v[20:21], v[70:71]
	ds_write2_b32 v31, v44, v45 offset1:1
	ds_write2_b32 v32, v14, v15 offset1:1
	s_waitcnt vmcnt(1)
	v_pk_mul_f32 v[14:15], v[42:43], v[76:77]
	v_pk_mul_f32 v[44:45], v[20:21], v[74:75]
	s_waitcnt vmcnt(0)
	v_pk_mul_f32 v[20:21], v[20:21], v[78:79]
	ds_write2_b32 v33, v44, v45 offset1:1
	ds_write2_b32 v37, v14, v15 offset1:1
	v_pk_mul_f32 v[14:15], v[42:43], v[80:81]
	ds_write2_b32 v38, v20, v21 offset1:1
	ds_write2_b32 v39, v14, v15 offset1:1
	s_waitcnt lgkmcnt(0)
	ds_read2_b32 v[14:15], v22 offset1:16
	ds_read2_b32 v[46:47], v22 offset0:33 offset1:49
	ds_read2_b32 v[48:49], v22 offset0:66 offset1:82
	ds_read2_b32 v[50:51], v22 offset0:99 offset1:115
	ds_read2_b32 v[58:59], v22 offset0:132 offset1:148
	ds_read2_b32 v[60:61], v22 offset0:165 offset1:181
	ds_read2_b32 v[62:63], v22 offset0:198 offset1:214
	ds_read2_b32 v[64:65], v22 offset0:231 offset1:247
	s_waitcnt lgkmcnt(6)
; #define LAS __attribute__((address_space(3)))
; #define LDS_WAIT() asm volatile("s_waitcnt lgkmcnt(0)" ::: "memory")
; __device__ __forceinline__ void transpose_item_i8(const float* W, int ldw, int K, unsigned char* WT8, LAS float* scr, int kb, int nb, int lane, const unsigned* CM, float* SW) {
;     ...
;     const int c = lane & 3;
; #pragma unroll
;     for (int j = 0; j < 2; ++j) { const int n = (lane >> 2) + 16 * j; const LAS float* sp = scr + (16 * c) * 33 + n;
;         v4u o; o.x = pk4_i8(sp[0 * 33], sp[1 * 33], sp[2 * 33], sp[3 * 33]); o.y = pk4_i8(sp[4 * 33], sp[5 * 33], sp[6 * 33], sp[7 * 33]);
;         o.z = pk4_i8(sp[8 * 33], sp[9 * 33], sp[10 * 33], sp[11 * 33]); o.w = pk4_i8(sp[12 * 33], sp[13 * 33], sp[14 * 33], sp[15 * 33]);
;         *(v4u*)(WT8 + (size_t)(n0 + n) * K + k0 + 16 * c) = o; }
;     LDS_WAIT();
	v_rndne_f32_e32 v41, v46
	v_rndne_f32_e32 v14, v14
	v_cvt_i32_f32_e32 v41, v41
	s_waitcnt lgkmcnt(5)
	v_rndne_f32_e32 v42, v48
	v_cvt_i32_f32_e32 v14, v14
	v_cvt_i32_f32_sdwa v42, v42 dst_sel:WORD_1 dst_unused:UNUSED_PAD src0_sel:DWORD
	s_waitcnt lgkmcnt(4)
	v_rndne_f32_e32 v43, v50
	v_cvt_i32_f32_sdwa v43, v43 dst_sel:BYTE_3 dst_unused:UNUSED_PAD src0_sel:DWORD
	v_lshlrev_b32_e32 v41, 8, v41
	v_perm_b32 v14, v41, v14, s36
	v_and_b32_e32 v41, 0xff0000, v42
	v_or3_b32 v42, v14, v41, v43
	s_waitcnt lgkmcnt(2)
	v_rndne_f32_e32 v41, v60
	v_rndne_f32_e32 v14, v58
	v_cvt_i32_f32_e32 v41, v41
	s_waitcnt lgkmcnt(1)
	v_rndne_f32_e32 v43, v62
	v_cvt_i32_f32_e32 v14, v14
	v_cvt_i32_f32_sdwa v43, v43 dst_sel:WORD_1 dst_unused:UNUSED_PAD src0_sel:DWORD
	s_waitcnt lgkmcnt(0)
	v_rndne_f32_e32 v44, v64
	v_cvt_i32_f32_sdwa v44, v44 dst_sel:BYTE_3 dst_unused:UNUSED_PAD src0_sel:DWORD
	ds_read2_b32 v[66:67], v40 offset0:8 offset1:24
	ds_read2_b32 v[68:69], v40 offset0:41 offset1:57
	ds_read2_b32 v[70:71], v40 offset0:74 offset1:90
	ds_read2_b32 v[72:73], v40 offset0:107 offset1:123
	v_lshlrev_b32_e32 v41, 8, v41
	v_perm_b32 v14, v41, v14, s36
	v_and_b32_e32 v41, 0xff0000, v43
	v_or3_b32 v43, v14, v41, v44
	s_waitcnt lgkmcnt(2)
	v_rndne_f32_e32 v41, v68
	v_rndne_f32_e32 v14, v66
	v_cvt_i32_f32_e32 v41, v41
	s_waitcnt lgkmcnt(1)
	v_rndne_f32_e32 v44, v70
	v_cvt_i32_f32_e32 v14, v14
	v_cvt_i32_f32_sdwa v44, v44 dst_sel:WORD_1 dst_unused:UNUSED_PAD src0_sel:DWORD
	s_waitcnt lgkmcnt(0)
	v_rndne_f32_e32 v45, v72
	v_cvt_i32_f32_sdwa v45, v45 dst_sel:BYTE_3 dst_unused:UNUSED_PAD src0_sel:DWORD
	ds_read2_b32 v[74:75], v40 offset0:140 offset1:156
	ds_read2_b32 v[76:77], v40 offset0:173 offset1:189
	ds_read2_b32 v[78:79], v40 offset0:206 offset1:222
	ds_read2_b32 v[80:81], v40 offset0:239 offset1:255
	v_lshlrev_b32_e32 v41, 8, v41
	v_perm_b32 v14, v41, v14, s36
	v_and_b32_e32 v41, 0xff0000, v44
	v_or3_b32 v44, v14, v41, v45
	s_waitcnt lgkmcnt(2)
	v_rndne_f32_e32 v41, v76
	v_rndne_f32_e32 v14, v74
	v_cvt_i32_f32_e32 v41, v41
	s_waitcnt lgkmcnt(1)
	v_rndne_f32_e32 v45, v78
	v_cvt_i32_f32_e32 v14, v14
	v_cvt_i32_f32_sdwa v45, v45 dst_sel:WORD_1 dst_unused:UNUSED_PAD src0_sel:DWORD
	s_waitcnt lgkmcnt(0)
	v_rndne_f32_e32 v46, v80
	v_cvt_i32_f32_sdwa v46, v46 dst_sel:BYTE_3 dst_unused:UNUSED_PAD src0_sel:DWORD
	v_lshlrev_b32_e32 v41, 8, v41
	v_perm_b32 v14, v41, v14, s36
	v_and_b32_e32 v41, 0xff0000, v45
	v_lshl_add_u64 v[20:21], v[12:13], 0, s[20:21]
	v_or3_b32 v45, v14, v41, v46
	v_lshlrev_b64 v[84:85], 11, v[82:83]
	v_rndne_f32_e32 v14, v15
	v_rndne_f32_e32 v15, v47
	v_lshl_add_u64 v[84:85], v[20:21], 0, v[84:85]
	v_cvt_i32_f32_e32 v15, v15
	v_rndne_f32_e32 v41, v49
	global_store_dwordx4 v[84:85], v[42:45], off
	v_cvt_i32_f32_e32 v14, v14
	v_cvt_i32_f32_sdwa v41, v41 dst_sel:WORD_1 dst_unused:UNUSED_PAD src0_sel:DWORD
	v_rndne_f32_e32 v42, v51
	v_cvt_i32_f32_sdwa v42, v42 dst_sel:BYTE_3 dst_unused:UNUSED_PAD src0_sel:DWORD
	v_lshlrev_b32_e32 v15, 8, v15
	v_perm_b32 v14, v15, v14, s36
	v_and_b32_e32 v15, 0xff0000, v41
	v_or3_b32 v42, v14, v15, v42
	v_rndne_f32_e32 v15, v61
	v_rndne_f32_e32 v14, v59
	v_cvt_i32_f32_e32 v15, v15
	v_rndne_f32_e32 v41, v63
	v_cvt_i32_f32_e32 v14, v14
	v_cvt_i32_f32_sdwa v41, v41 dst_sel:WORD_1 dst_unused:UNUSED_PAD src0_sel:DWORD
	v_rndne_f32_e32 v43, v65
	v_cvt_i32_f32_sdwa v43, v43 dst_sel:BYTE_3 dst_unused:UNUSED_PAD src0_sel:DWORD
	v_lshlrev_b32_e32 v15, 8, v15
	v_perm_b32 v14, v15, v14, s36
	v_and_b32_e32 v15, 0xff0000, v41
	v_or3_b32 v43, v14, v15, v43
	v_rndne_f32_e32 v15, v69
	v_rndne_f32_e32 v14, v67
	v_cvt_i32_f32_e32 v15, v15
	v_rndne_f32_e32 v41, v71
	v_cvt_i32_f32_e32 v14, v14
	v_cvt_i32_f32_sdwa v41, v41 dst_sel:WORD_1 dst_unused:UNUSED_PAD src0_sel:DWORD
	v_rndne_f32_e32 v44, v73
	v_cvt_i32_f32_sdwa v44, v44 dst_sel:BYTE_3 dst_unused:UNUSED_PAD src0_sel:DWORD
	v_lshlrev_b32_e32 v15, 8, v15
	v_perm_b32 v14, v15, v14, s36
	v_and_b32_e32 v15, 0xff0000, v41
	v_or3_b32 v44, v14, v15, v44
	v_rndne_f32_e32 v15, v77
	v_rndne_f32_e32 v14, v75
	v_cvt_i32_f32_e32 v15, v15
	v_rndne_f32_e32 v41, v79
	v_cvt_i32_f32_e32 v14, v14
	v_cvt_i32_f32_sdwa v41, v41 dst_sel:WORD_1 dst_unused:UNUSED_PAD src0_sel:DWORD
	v_rndne_f32_e32 v45, v81
	v_cvt_i32_f32_sdwa v45, v45 dst_sel:BYTE_3 dst_unused:UNUSED_PAD src0_sel:DWORD
	v_lshlrev_b32_e32 v15, 8, v15
	v_perm_b32 v14, v15, v14, s36
	v_and_b32_e32 v15, 0xff0000, v41
	v_or3_b32 v45, v14, v15, v45
	v_add_u32_e32 v14, 16, v82
	v_ashrrev_i32_e32 v15, 31, v14
	v_lshlrev_b64 v[14:15], 11, v[14:15]
	v_lshl_add_u64 v[14:15], v[20:21], 0, v[14:15]
	global_store_dwordx4 v[14:15], v[42:45], off
	s_waitcnt lgkmcnt(0)
	s_cbranch_scc1 .LBB0_151
